# top-k threshold bisection: compare masks rotate over four SGPR pairs instead of VCC (on top of hand-written late conversion + pool/conv pass)
# baseline (speedup 1.0000x reference)
; template <int J0, int J1> __device__ __forceinline__ int cnt_ge(const unsigned (&key)[32], unsigned cand) {
;     int c = 0;
; #pragma unroll
;     for (int j = J0; j < J1; ++j) c += __popcll(__ballot(key[j] >= cand));
;     return c;
; }
; __device__ __forceinline__ void select_row(Frame& F, int row, int lane_, const LAS float* srl) {
;     ...
;             if (clo - chi <= 64) break;
;             const unsigned cand = T | (1u << bit);
;             int c = cnt_ge<0, 8>(key, cand);
;             if (nj > 8) { c += cnt_ge<8, 16>(key, cand); if (nj > 16) { c += cnt_ge<16, 24>(key, cand); if (nj > 24) c += cnt_ge<24, 32>(key, cand); } }
;             if (c >= TOPK) { T = cand; clo = c; if (c == TOPK) { exact = true; break; } } else chi = c;
.LBB0_274:
	s_lshl_b32 s6, 1, s18
	s_or_b32 s22, s6, s20
	v_cmp_le_u32_e64 s[44:45], s22, v17
	s_bcnt1_i32_b64 s6, s[44:45]
	v_cmp_le_u32_e64 s[46:47], s22, v23
	s_bcnt1_i32_b64 s7, s[46:47]
	v_cmp_le_u32_e64 s[48:49], s22, v24
	s_add_i32 s6, s7, s6
	s_bcnt1_i32_b64 s7, s[48:49]
	v_cmp_le_u32_e64 s[50:51], s22, v25
	s_add_i32 s6, s6, s7
	s_bcnt1_i32_b64 s7, s[50:51]
	v_cmp_le_u32_e64 s[44:45], s22, v26
	s_add_i32 s6, s6, s7
	s_bcnt1_i32_b64 s7, s[44:45]
	v_cmp_le_u32_e64 s[46:47], s22, v27
	s_add_i32 s6, s6, s7
	s_bcnt1_i32_b64 s7, s[46:47]
	v_cmp_le_u32_e64 s[48:49], s22, v28
	s_add_i32 s6, s6, s7
	s_bcnt1_i32_b64 s7, s[48:49]
	v_cmp_le_u32_e64 s[50:51], s22, v29
	s_add_i32 s6, s6, s7
	s_bcnt1_i32_b64 s7, s[50:51]
	v_cndmask_b32_e64 v18, 0, 1, s[4:5]
	s_add_i32 s38, s6, s7
	v_cmp_ne_u32_e64 s[36:37], 1, v18
	s_andn2_b64 vcc, exec, s[4:5]
	s_cbranch_vccnz .LBB0_278
	v_cmp_le_u32_e64 s[44:45], s22, v30
	s_bcnt1_i32_b64 s6, s[44:45]
	v_cmp_le_u32_e64 s[46:47], s22, v31
	s_bcnt1_i32_b64 s7, s[46:47]
	v_cmp_le_u32_e64 s[48:49], s22, v32
	s_add_i32 s6, s38, s6
	s_bcnt1_i32_b64 s21, s[48:49]
	v_cmp_le_u32_e64 s[50:51], s22, v33
	s_add_i32 s6, s6, s7
	s_bcnt1_i32_b64 s39, s[50:51]
	v_cmp_le_u32_e64 s[44:45], s22, v34
	s_add_i32 s6, s6, s21
	s_bcnt1_i32_b64 s40, s[44:45]
	v_cmp_le_u32_e64 s[46:47], s22, v35
	s_add_i32 s6, s6, s39
	s_bcnt1_i32_b64 s41, s[46:47]
	v_cmp_le_u32_e64 s[48:49], s22, v36
	s_add_i32 s6, s6, s40
	s_bcnt1_i32_b64 s42, s[48:49]
	v_cmp_le_u32_e64 s[50:51], s22, v37
	s_add_i32 s6, s6, s41
	s_bcnt1_i32_b64 s43, s[50:51]
	s_add_i32 s6, s6, s42
	s_andn2_b64 vcc, exec, s[16:17]
	s_add_i32 s38, s6, s43
	s_cbranch_vccnz .LBB0_278
	v_cmp_le_u32_e64 s[44:45], s22, v38
	s_bcnt1_i32_b64 s6, s[44:45]
	v_cmp_le_u32_e64 s[46:47], s22, v39
	s_bcnt1_i32_b64 s7, s[46:47]
	v_cmp_le_u32_e64 s[48:49], s22, v40
	s_add_i32 s6, s38, s6
	s_bcnt1_i32_b64 s21, s[48:49]
	v_cmp_le_u32_e64 s[50:51], s22, v41
	s_add_i32 s6, s6, s7
	s_bcnt1_i32_b64 s39, s[50:51]
	v_cmp_le_u32_e64 s[44:45], s22, v42
	s_add_i32 s6, s6, s21
	s_bcnt1_i32_b64 s40, s[44:45]
	v_cmp_le_u32_e64 s[46:47], s22, v43
	s_add_i32 s6, s6, s39
	s_bcnt1_i32_b64 s41, s[46:47]
	v_cmp_le_u32_e64 s[48:49], s22, v44
	s_add_i32 s6, s6, s40
	s_bcnt1_i32_b64 s42, s[48:49]
	v_cmp_le_u32_e64 s[50:51], s22, v45
	s_add_i32 s6, s6, s41
	s_bcnt1_i32_b64 s43, s[50:51]
	s_add_i32 s6, s6, s42
	s_andn2_b64 vcc, exec, s[72:73]
	s_add_i32 s38, s6, s43
	s_cbranch_vccnz .LBB0_278
	v_cmp_le_u32_e64 s[44:45], s22, v46
	s_bcnt1_i32_b64 s6, s[44:45]
	v_cmp_le_u32_e64 s[46:47], s22, v47
	s_bcnt1_i32_b64 s7, s[46:47]
	v_cmp_le_u32_e64 s[48:49], s22, v48
	s_add_i32 s6, s38, s6
	s_bcnt1_i32_b64 s21, s[48:49]
	v_cmp_le_u32_e64 s[50:51], s22, v49
	s_add_i32 s6, s6, s7
	s_bcnt1_i32_b64 s39, s[50:51]
	v_cmp_le_u32_e64 s[44:45], s22, v20
	s_add_i32 s6, s6, s21
	s_bcnt1_i32_b64 s40, s[44:45]
	v_cmp_le_u32_e64 s[46:47], s22, v21
	s_add_i32 s6, s6, s39
	s_bcnt1_i32_b64 s41, s[46:47]
	v_cmp_le_u32_e64 s[48:49], s22, v50
	s_add_i32 s6, s6, s40
	s_bcnt1_i32_b64 s42, s[48:49]
	v_cmp_le_u32_e64 s[50:51], s22, v51
	s_add_i32 s6, s6, s41
	s_bcnt1_i32_b64 s43, s[50:51]
	s_add_i32 s6, s6, s42
	s_add_i32 s38, s6, s43

; template <int J0, int J1> __device__ __forceinline__ int cnt_ge(const unsigned (&key)[32], unsigned cand) {
;     int c = 0;
; #pragma unroll
;     for (int j = J0; j < J1; ++j) c += __popcll(__ballot(key[j] >= cand));
;     return c;
; }
; __device__ __forceinline__ void select_row(Frame& F, int row, int lane_, const LAS float* srl) {
;     ...
;             if (clo - chi <= 64) break;
;             const unsigned cand = T | (1u << bit);
;             int c = cnt_ge<0, 8>(key, cand);
;             if (nj > 8) { c += cnt_ge<8, 16>(key, cand); if (nj > 16) { c += cnt_ge<16, 24>(key, cand); if (nj > 24) c += cnt_ge<24, 32>(key, cand); } }
;             if (c >= TOPK) { T = cand; clo = c; if (c == TOPK) { exact = true; break; } } else chi = c;
.LBB0_381:
	s_lshl_b32 s0, 1, s18
	s_or_b32 s22, s0, s20
	v_cmp_le_u32_e64 s[44:45], s22, v20
	s_bcnt1_i32_b64 s0, s[44:45]
	v_cmp_le_u32_e64 s[46:47], s22, v21
	s_bcnt1_i32_b64 s1, s[46:47]
	v_cmp_le_u32_e64 s[48:49], s22, v22
	s_add_i32 s0, s1, s0
	s_bcnt1_i32_b64 s1, s[48:49]
	v_cmp_le_u32_e64 s[50:51], s22, v23
	s_add_i32 s0, s0, s1
	s_bcnt1_i32_b64 s1, s[50:51]
	v_cmp_le_u32_e64 s[44:45], s22, v24
	s_add_i32 s0, s0, s1
	s_bcnt1_i32_b64 s1, s[44:45]
	v_cmp_le_u32_e64 s[46:47], s22, v25
	s_add_i32 s0, s0, s1
	s_bcnt1_i32_b64 s1, s[46:47]
	v_cmp_le_u32_e64 s[48:49], s22, v26
	s_add_i32 s0, s0, s1
	s_bcnt1_i32_b64 s1, s[48:49]
	v_cmp_le_u32_e64 s[50:51], s22, v27
	s_add_i32 s0, s0, s1
	s_bcnt1_i32_b64 s1, s[50:51]
	v_cndmask_b32_e64 v16, 0, 1, s[4:5]
	s_add_i32 s38, s0, s1
	v_cmp_ne_u32_e64 s[36:37], 1, v16
	s_andn2_b64 vcc, exec, s[4:5]
	s_cbranch_vccnz .LBB0_385
	v_cmp_le_u32_e64 s[44:45], s22, v28
	s_bcnt1_i32_b64 s0, s[44:45]
	v_cmp_le_u32_e64 s[46:47], s22, v29
	s_bcnt1_i32_b64 s1, s[46:47]
	v_cmp_le_u32_e64 s[48:49], s22, v30
	s_add_i32 s0, s38, s0
	s_bcnt1_i32_b64 s6, s[48:49]
	v_cmp_le_u32_e64 s[50:51], s22, v31
	s_add_i32 s0, s0, s1
	s_bcnt1_i32_b64 s7, s[50:51]
	v_cmp_le_u32_e64 s[44:45], s22, v32
	s_add_i32 s0, s0, s6
	s_bcnt1_i32_b64 s8, s[44:45]
	v_cmp_le_u32_e64 s[46:47], s22, v33
	s_add_i32 s0, s0, s7
	s_bcnt1_i32_b64 s10, s[46:47]
	v_cmp_le_u32_e64 s[48:49], s22, v34
	s_add_i32 s0, s0, s8
	s_bcnt1_i32_b64 s11, s[48:49]
	v_cmp_le_u32_e64 s[50:51], s22, v35
	s_add_i32 s0, s0, s10
	s_bcnt1_i32_b64 s19, s[50:51]
	s_add_i32 s0, s0, s11
	s_andn2_b64 vcc, exec, s[16:17]
	s_add_i32 s38, s0, s19
	s_cbranch_vccnz .LBB0_385
	v_cmp_le_u32_e64 s[44:45], s22, v36
	s_bcnt1_i32_b64 s0, s[44:45]
	v_cmp_le_u32_e64 s[46:47], s22, v37
	s_bcnt1_i32_b64 s1, s[46:47]
	v_cmp_le_u32_e64 s[48:49], s22, v38
	s_add_i32 s0, s38, s0
	s_bcnt1_i32_b64 s6, s[48:49]
	v_cmp_le_u32_e64 s[50:51], s22, v39
	s_add_i32 s0, s0, s1
	s_bcnt1_i32_b64 s7, s[50:51]
	v_cmp_le_u32_e64 s[44:45], s22, v40
	s_add_i32 s0, s0, s6
	s_bcnt1_i32_b64 s8, s[44:45]
	v_cmp_le_u32_e64 s[46:47], s22, v41
	s_add_i32 s0, s0, s7
	s_bcnt1_i32_b64 s10, s[46:47]
	v_cmp_le_u32_e64 s[48:49], s22, v42
	s_add_i32 s0, s0, s8
	s_bcnt1_i32_b64 s11, s[48:49]
	v_cmp_le_u32_e64 s[50:51], s22, v43
	s_add_i32 s0, s0, s10
	s_bcnt1_i32_b64 s19, s[50:51]
	s_add_i32 s0, s0, s11
	s_andn2_b64 vcc, exec, s[68:69]
	s_add_i32 s38, s0, s19
	s_cbranch_vccnz .LBB0_385
	v_cmp_le_u32_e64 s[44:45], s22, v44
	s_bcnt1_i32_b64 s0, s[44:45]
	v_cmp_le_u32_e64 s[46:47], s22, v45
	s_bcnt1_i32_b64 s1, s[46:47]
	v_cmp_le_u32_e64 s[48:49], s22, v46
	s_add_i32 s0, s38, s0
	s_bcnt1_i32_b64 s6, s[48:49]
	v_cmp_le_u32_e64 s[50:51], s22, v47
	s_add_i32 s0, s0, s1
	s_bcnt1_i32_b64 s7, s[50:51]
	v_cmp_le_u32_e64 s[44:45], s22, v18
	s_add_i32 s0, s0, s6
	s_bcnt1_i32_b64 s8, s[44:45]
	v_cmp_le_u32_e64 s[46:47], s22, v19
	s_add_i32 s0, s0, s7
	s_bcnt1_i32_b64 s10, s[46:47]
	v_cmp_le_u32_e64 s[48:49], s22, v48
	s_add_i32 s0, s0, s8
	s_bcnt1_i32_b64 s11, s[48:49]
	v_cmp_le_u32_e64 s[50:51], s22, v49
	s_add_i32 s0, s0, s10
	s_bcnt1_i32_b64 s19, s[50:51]
	s_add_i32 s0, s0, s11
	s_add_i32 s38, s0, s19
